# layer-1 next-layer weight conversion on 128 workgroups instead of 64 (plus v1 barrier edit)
# speedup vs baseline: 1.0184x; 1.0046x over previous
.LBB0_1236:
	s_cmp_lt_i32 s12, 14
	s_cselect_b64 s[0:1], -1, 0
	s_cmp_gt_i32 s13, 13
	s_cselect_b64 s[2:3], -1, 0
	s_and_b64 s[0:1], s[0:1], s[2:3]
	s_andn2_b64 vcc, exec, s[0:1]
	s_cbranch_vccnz .LBB0_1483
	v_readlane_b32 s0, v254, 0
	v_mbcnt_lo_u32_b32 v0, -1, 0
	s_cmp_gt_i32 s0, 0x7f
	v_mbcnt_hi_u32_b32 v26, -1, v0
	s_cbranch_scc1 .LBB0_1394
	v_readlane_b32 s0, v254, 0
	s_lshl_b32 s0, s0, 3
	v_readlane_b32 s1, v254, 41
	s_min_i32 s5, s74, 0x80
	s_add_i32 s6, s1, s0
	s_lshl_b32 s4, s5, 3
	s_waitcnt lgkmcnt(0)
	v_mov_b32_e32 v14, v26
	s_cmpk_gt_i32 s6, 0x6a7f
	s_cbranch_scc1 .LBB0_1333
	s_add_u32 s7, s90, 0x800000
	s_addc_u32 s70, s91, 0
	s_add_u32 s71, s90, 0xe00000
	s_addc_u32 s75, s91, 0
	s_add_u32 s92, s90, 0x1000000
	s_addc_u32 s93, s91, 0
	s_add_u32 s0, s90, 0x5000000
	v_writelane_b32 v255, s0, 1
	s_addc_u32 s0, s91, 0
	v_writelane_b32 v255, s0, 2
	s_add_u32 s0, s90, 0x7000000
	v_writelane_b32 v255, s0, 6
	s_addc_u32 s0, s91, 0
	v_writelane_b32 v255, s0, 7
	s_add_u32 s0, s90, 0x7200000
	v_writelane_b32 v255, s0, 8
	s_addc_u32 s0, s91, 0
	v_writelane_b32 v255, s0, 9
	s_add_u32 s0, s78, 0x8000000
	v_writelane_b32 v255, s0, 3
	s_addc_u32 s0, s79, 0
	s_add_u32 s95, s80, 0x8000000
	v_writelane_b32 v255, s0, 4
	s_addc_u32 s29, s81, 0
	v_readlane_b32 s0, v254, 41
	s_add_u32 s30, s82, 0x8000000
	s_mulk_i32 s0, 0x2100
	s_addc_u32 s31, s83, 0
	s_add_i32 s0, s0, 0
	s_add_u32 s2, s86, 0x200000
	v_writelane_b32 v255, s2, 10
	s_addc_u32 s2, s87, 0
	v_writelane_b32 v255, s2, 11
	s_add_u32 s2, s84, 0x800000
	v_writelane_b32 v255, s2, 12
	s_addc_u32 s2, s85, 0
	v_writelane_b32 v255, s2, 13
	v_ashrrev_i32_e32 v0, 5, v14
	v_and_b32_e32 v2, 31, v14
	s_movk_i32 s2, 0x84
	v_lshlrev_b32_e32 v4, 2, v2
	v_mul_lo_u32 v5, v0, s2
	v_add3_u32 v15, s0, v4, v5
	v_and_b32_e32 v5, 7, v14
	v_ashrrev_i32_e32 v4, 3, v14
	v_lshlrev_b32_e32 v6, 3, v5
	v_mul_u32_u24_e32 v5, 0x420, v5
	v_lshlrev_b32_e32 v8, 2, v4
	v_add3_u32 v16, s0, v5, v8
	s_lshl_b32 s0, s6, 1
	s_add_i32 s57, s0, 0xfffff400
	s_lshl_b32 s0, s6, 6
	s_add_i32 s55, s0, 0xfffe8000
	s_lshl_b32 s0, s6, 2
	s_add_i32 s35, s0, 0xffffe800
	s_lshl_b32 s0, s5, 9
	s_mov_b32 s33, s0
	s_add_i32 s56, s0, 0xffff4000
	s_lshl_b32 s0, s5, 10
	v_mov_b32_e32 v3, 0
	v_add_u32_e32 v8, 8, v4
	v_add_u32_e32 v10, 16, v4
	v_add_u32_e32 v12, 24, v4
	s_mul_i32 s69, s5, 24
	v_writelane_b32 v254, s0, 61
	s_lshl_b32 s0, s5, 6
	s_lshl_b32 s59, s5, 8
	s_mov_b32 s1, 0
	v_ashrrev_i32_e32 v1, 31, v0
	v_mov_b32_e32 v7, v3
	v_ashrrev_i32_e32 v5, 31, v4
	v_ashrrev_i32_e32 v9, 31, v8
	v_ashrrev_i32_e32 v11, 31, v10
	v_ashrrev_i32_e32 v13, 31, v12
	s_lshl_b32 s94, s6, 5
	s_lshl_b32 s28, s69, 5
	s_lshl_b32 s58, s69, 1
	s_lshl_b32 s34, s69, 6
	s_lshl_b32 s52, s69, 2
	s_lshl_b32 s53, s5, 4
	s_lshl_b32 s54, s5, 5
	v_writelane_b32 v254, s0, 63
	s_add_i32 s59, s59, 0xffff4000
	v_lshlrev_b32_e32 v2, 2, v2
	s_mov_b32 s60, 0xc3e00000
	v_mov_b32_e32 v17, 0x43e00000
	s_mov_b32 s61, s6
	s_branch .LBB0_1243
